# v41: v34 + attention tile: mask-select ops of the second score block moved into the shadow of the first block's QK MFMAs (MFMA/VALU interleave)
# speedup vs baseline: 1.0037x; 1.0037x over previous
; __device__ __forceinline__ float xor32_max(float x) { float lo, hi; xor32_pair(x, lo, hi); return fmaxf(lo, hi); }
; #define AT_LDK(dst, kb_i, g_) do { _Pragma("unroll") for (int q_ = 0; q_ < 4; ++q_) dst[q_] = *(const LAS bf16x8*)(kb_ + (kb_i) * 32 * AT_KSTR + (4 * (g_) + q_) * 32); } while (0)
; #define AT_MMK(kb_i, src, g_) do { _Pragma("unroll") for (int q_ = 0; q_ < 4; ++q_) p[kb_i] = __builtin_amdgcn_mfma_f32_32x32x16_bf16(src[q_], qf[4 * (g_) + q_], p[kb_i], 0, 0, 0); } while (0)
; __device__ __forceinline__ void attn_block(Frame& F, int b, int g, int qb, float sbound) {
;     ...
;             for (int kb = 0; kb < 2; ++kb) { const unsigned mword = (kb ? mw.y : mw.x) >> (4 * hi);
; #pragma unroll
;                 for (int r = 0; r < 16; ++r) { const int ko = (r & 3) + 8 * (r >> 2);
;                     const unsigned tm = (unsigned)__builtin_amdgcn_sbfe((int)mword, ko, 1);
;                     p[kb][r] = __builtin_bit_cast(float, (__builtin_bit_cast(unsigned, slope2 * (float)(32 * kb + ko)) & tm) | (__builtin_bit_cast(unsigned, -2e30f) & ~tm)); } }
;             {
;                 bf16x8 ka[4], kc[4];
;     ...
;                 AT_LDK(ka, 0, 0); __builtin_amdgcn_sched_barrier(0); AT_MMK(0, ka, 0); __builtin_amdgcn_sched_barrier(0);
;                 AT_LDK(kc, 0, 1); __builtin_amdgcn_sched_barrier(0); AT_MMK(0, kc, 1); __builtin_amdgcn_sched_barrier(0);
;                 AT_LDK(ka, 1, 0); __builtin_amdgcn_sched_barrier(0); AT_MMK(1, ka, 0); __builtin_amdgcn_sched_barrier(0);
;                 AT_LDK(kc, 1, 1); __builtin_amdgcn_sched_barrier(0); AT_MMK(1, kc, 1); __builtin_amdgcn_sched_barrier(0);
;     ...
;             }
;             const float base = -slope2 * (float)(t - 64 * kt - 4 * hi);
;             float rmax = -3e30f;
; #pragma unroll
;             for (int kb = 0; kb < 2; ++kb)
; #pragma unroll
;                 for (int r = 0; r < 16; ++r) rmax = fmaxf(rmax, p[kb][r]);
;             rmax += base; rmax = xor32_max(rmax);
;             const float mn = fmaxf(m, rmax), alpha = __builtin_amdgcn_exp2f(m - mn), mrel = mn - base;
;             const bool moved = __any(mn != m);
;             m = mn;
.LBB0_1307:
	s_and_b64 vcc, exec, s[42:43]
	s_cbranch_vccnz .LBB0_1311
	s_mul_i32 s0, s35, 0x4400
	s_add_i32 s0, s0, 0
	v_lshrrev_b32_e32 v38, v192, v223
	v_add3_u32 v240, s0, v225, v226
	v_bfe_i32 v100, v38, 0, 1
	v_bfe_i32 v101, v38, 1, 1
	v_bfe_i32 v102, v38, 2, 1
	v_bfe_i32 v103, v38, 3, 1
	v_bfe_i32 v104, v38, 8, 1
	v_bfe_i32 v105, v38, 9, 1
	v_bfe_i32 v106, v38, 10, 1
	v_bfe_i32 v107, v38, 11, 1
	v_bfe_i32 v108, v38, 16, 1
	v_bfe_i32 v109, v38, 17, 1
	v_bfe_i32 v110, v38, 18, 1
	v_bfe_i32 v111, v38, 19, 1
	v_bfe_i32 v112, v38, 24, 1
	v_bfe_i32 v113, v38, 25, 1
	v_bfe_i32 v114, v38, 26, 1
	v_bfe_i32 v115, v38, 27, 1
	ds_read_b128 v[38:41], v240
	ds_read_b128 v[42:45], v240 offset:32
	ds_read_b128 v[46:49], v240 offset:64
	ds_read_b128 v[236:239], v240 offset:96
	v_lshrrev_b32_e32 v34, v192, v222
	v_bfe_i32 v116, v34, 0, 1
	v_bfe_i32 v117, v34, 1, 1
	v_bfe_i32 v118, v34, 2, 1
	v_bfe_i32 v119, v34, 3, 1
	v_bfe_i32 v120, v34, 8, 1
	v_bfe_i32 v121, v34, 9, 1
	v_bfe_i32 v122, v34, 10, 1
	v_bfe_i32 v123, v34, 11, 1
	v_bfe_i32 v124, v34, 16, 1
	v_bfe_i32 v125, v34, 17, 1
	v_bfe_i32 v126, v34, 18, 1
	v_bfe_i32 v127, v34, 19, 1
	v_bfe_i32 v128, v34, 24, 1
	v_bfe_i32 v129, v34, 25, 1
	v_bfe_i32 v130, v34, 26, 1
	v_bfe_i32 v34, v34, 27, 1
	v_bitop3_b32 v131, v217, s50, v34 bitop3:0xe4
	v_bitop3_b32 v130, v216, s50, v130 bitop3:0xe4
	v_bitop3_b32 v129, v215, s50, v129 bitop3:0xe4
	v_bitop3_b32 v128, v214, s50, v128 bitop3:0xe4
	v_bitop3_b32 v127, v213, s50, v127 bitop3:0xe4
	v_bitop3_b32 v126, v212, s50, v126 bitop3:0xe4
	v_bitop3_b32 v125, v211, s50, v125 bitop3:0xe4
	v_bitop3_b32 v124, v210, s50, v124 bitop3:0xe4
	v_bitop3_b32 v123, v209, s50, v123 bitop3:0xe4
	v_bitop3_b32 v122, v208, s50, v122 bitop3:0xe4
	v_bitop3_b32 v121, v207, s50, v121 bitop3:0xe4
	v_bitop3_b32 v120, v206, s50, v120 bitop3:0xe4
	v_bitop3_b32 v119, v205, s50, v119 bitop3:0xe4
	v_bitop3_b32 v118, v204, s50, v118 bitop3:0xe4
	v_bitop3_b32 v117, v1, s50, v117 bitop3:0xe4
	v_bitop3_b32 v116, v50, s50, v116 bitop3:0xe4
	s_waitcnt lgkmcnt(3)
	s_nop 0
	v_mfma_f32_32x32x16_bf16 v[116:131], v[38:41], v[132:135], v[116:131]
	v_bitop3_b32 v115, v33, s50, v115 bitop3:0xe4
	v_bitop3_b32 v114, v32, s50, v114 bitop3:0xe4
	v_bitop3_b32 v113, v31, s50, v113 bitop3:0xe4
	v_bitop3_b32 v112, v30, s50, v112 bitop3:0xe4
	s_waitcnt lgkmcnt(2)
	v_mfma_f32_32x32x16_bf16 v[116:131], v[42:45], v[136:139], v[116:131]
	v_bitop3_b32 v111, v29, s50, v111 bitop3:0xe4
	v_bitop3_b32 v110, v28, s50, v110 bitop3:0xe4
	v_bitop3_b32 v109, v27, s50, v109 bitop3:0xe4
	v_bitop3_b32 v108, v26, s50, v108 bitop3:0xe4
	s_waitcnt lgkmcnt(1)
	v_mfma_f32_32x32x16_bf16 v[116:131], v[46:49], v[140:143], v[116:131]
	v_bitop3_b32 v107, v25, s50, v107 bitop3:0xe4
	v_bitop3_b32 v106, v24, s50, v106 bitop3:0xe4
	v_bitop3_b32 v105, v23, s50, v105 bitop3:0xe4
	v_bitop3_b32 v104, v22, s50, v104 bitop3:0xe4
	s_waitcnt lgkmcnt(0)
	v_mfma_f32_32x32x16_bf16 v[116:131], v[236:239], v[144:147], v[116:131]
	v_bitop3_b32 v103, v21, s50, v103 bitop3:0xe4
	v_bitop3_b32 v102, v20, s50, v102 bitop3:0xe4
	v_bitop3_b32 v101, v19, s50, v101 bitop3:0xe4
	v_bitop3_b32 v100, v18, s50, v100 bitop3:0xe4
	ds_read_b128 v[38:41], v240 offset:128
	ds_read_b128 v[42:45], v240 offset:160
	ds_read_b128 v[46:49], v240 offset:192
	ds_read_b128 v[236:239], v240 offset:224
	s_waitcnt lgkmcnt(3)
	v_mfma_f32_32x32x16_bf16 v[116:131], v[38:41], v[148:151], v[116:131]
	s_waitcnt lgkmcnt(2)
	v_mfma_f32_32x32x16_bf16 v[116:131], v[42:45], v[152:155], v[116:131]
	s_waitcnt lgkmcnt(1)
	v_mfma_f32_32x32x16_bf16 v[116:131], v[46:49], v[156:159], v[116:131]
	s_waitcnt lgkmcnt(0)
	v_mfma_f32_32x32x16_bf16 v[116:131], v[236:239], v[160:163], v[116:131]
	ds_read_b128 v[38:41], v240 offset:8704
	ds_read_b128 v[42:45], v240 offset:8736
	ds_read_b128 v[46:49], v240 offset:8768
	ds_read_b128 v[236:239], v240 offset:8800
	s_waitcnt lgkmcnt(3)
	v_mfma_f32_32x32x16_bf16 v[100:115], v[38:41], v[132:135], v[100:115]
	s_waitcnt lgkmcnt(2)
	v_mfma_f32_32x32x16_bf16 v[100:115], v[42:45], v[136:139], v[100:115]
	s_waitcnt lgkmcnt(1)
	v_mfma_f32_32x32x16_bf16 v[100:115], v[46:49], v[140:143], v[100:115]
	s_waitcnt lgkmcnt(0)
	v_mfma_f32_32x32x16_bf16 v[100:115], v[236:239], v[144:147], v[100:115]
	ds_read_b128 v[38:41], v240 offset:8832
	ds_read_b128 v[42:45], v240 offset:8864
	ds_read_b128 v[46:49], v240 offset:8896
	ds_read_b128 v[236:239], v240 offset:8928
	s_waitcnt lgkmcnt(3)
	v_mfma_f32_32x32x16_bf16 v[100:115], v[38:41], v[148:151], v[100:115]
	s_waitcnt lgkmcnt(2)
	v_mfma_f32_32x32x16_bf16 v[100:115], v[42:45], v[152:155], v[100:115]
	s_waitcnt lgkmcnt(1)
	v_mfma_f32_32x32x16_bf16 v[100:115], v[46:49], v[156:159], v[100:115]
	s_waitcnt lgkmcnt(0)
	v_mfma_f32_32x32x16_bf16 v[100:115], v[236:239], v[160:163], v[100:115]
	v_add_u32_e32 v34, s56, v228
	v_cvt_f32_i32_e32 v39, v34
	v_max3_f32 v34, v116, s51, v117
	v_max3_f32 v34, v34, v118, v119
	v_max3_f32 v34, v34, v120, v121
	v_max3_f32 v34, v34, v122, v123
	v_max3_f32 v34, v34, v124, v125
	v_max3_f32 v34, v34, v126, v127
	v_max3_f32 v34, v34, v128, v129
	v_max3_f32 v34, v34, v130, v131
	s_nop 1
	v_max3_f32 v34, v34, v100, v101
	v_max3_f32 v34, v34, v102, v103
	v_max3_f32 v34, v34, v104, v105
	v_max3_f32 v34, v34, v106, v107
	v_max3_f32 v34, v34, v108, v109
	v_max3_f32 v34, v34, v110, v111
	v_max3_f32 v34, v34, v112, v113
	v_max3_f32 v34, v34, v114, v115
	v_fma_f32 v34, -v1, v39, v34
	v_mov_b32_e32 v38, v34
	s_nop 1
	v_permlane32_swap_b32 v34, v38
	s_nop 0
	v_max3_f32 v38, v235, v34, v38
	v_sub_f32_e32 v34, v235, v38
	v_exp_f32_e32 v34, v34
	v_cmp_neq_f32_e32 vcc, v38, v235
	s_cbranch_vccz .LBB0_1310
; __device__ __forceinline__ void attn_block(Frame& F, int b, int g, int qb, float sbound) {
;     ...
;             if (moved) {
; #pragma unroll
;                 for (int db = 0; db < 4; ++db)
; #pragma unroll
;                     for (int r = 0; r < 16; ++r) o[db][r] *= alpha;
;             }
	v_pk_mul_f32 v[98:99], v[98:99], v[34:35] op_sel_hi:[1,0]
	v_pk_mul_f32 v[96:97], v[96:97], v[34:35] op_sel_hi:[1,0]
	v_pk_mul_f32 v[94:95], v[94:95], v[34:35] op_sel_hi:[1,0]
	v_pk_mul_f32 v[92:93], v[92:93], v[34:35] op_sel_hi:[1,0]
	v_pk_mul_f32 v[90:91], v[90:91], v[34:35] op_sel_hi:[1,0]
	v_pk_mul_f32 v[88:89], v[88:89], v[34:35] op_sel_hi:[1,0]
	v_pk_mul_f32 v[86:87], v[86:87], v[34:35] op_sel_hi:[1,0]
	v_pk_mul_f32 v[84:85], v[84:85], v[34:35] op_sel_hi:[1,0]
	v_pk_mul_f32 v[82:83], v[82:83], v[34:35] op_sel_hi:[1,0]
	v_pk_mul_f32 v[80:81], v[80:81], v[34:35] op_sel_hi:[1,0]
	v_pk_mul_f32 v[78:79], v[78:79], v[34:35] op_sel_hi:[1,0]
	v_pk_mul_f32 v[76:77], v[76:77], v[34:35] op_sel_hi:[1,0]
	v_pk_mul_f32 v[74:75], v[74:75], v[34:35] op_sel_hi:[1,0]
	v_pk_mul_f32 v[72:73], v[72:73], v[34:35] op_sel_hi:[1,0]
	v_pk_mul_f32 v[70:71], v[70:71], v[34:35] op_sel_hi:[1,0]
	v_pk_mul_f32 v[68:69], v[68:69], v[34:35] op_sel_hi:[1,0]
	v_pk_mul_f32 v[66:67], v[66:67], v[34:35] op_sel_hi:[1,0]
	v_pk_mul_f32 v[64:65], v[64:65], v[34:35] op_sel_hi:[1,0]
	v_pk_mul_f32 v[62:63], v[62:63], v[34:35] op_sel_hi:[1,0]
	v_pk_mul_f32 v[60:61], v[60:61], v[34:35] op_sel_hi:[1,0]
	v_pk_mul_f32 v[58:59], v[58:59], v[34:35] op_sel_hi:[1,0]
	v_pk_mul_f32 v[56:57], v[56:57], v[34:35] op_sel_hi:[1,0]
	v_pk_mul_f32 v[54:55], v[54:55], v[34:35] op_sel_hi:[1,0]
	v_pk_mul_f32 v[52:53], v[52:53], v[34:35] op_sel_hi:[1,0]
	v_pk_mul_f32 v[16:17], v[16:17], v[34:35] op_sel_hi:[1,0]
	v_pk_mul_f32 v[14:15], v[14:15], v[34:35] op_sel_hi:[1,0]
	v_pk_mul_f32 v[12:13], v[12:13], v[34:35] op_sel_hi:[1,0]
	v_pk_mul_f32 v[10:11], v[10:11], v[34:35] op_sel_hi:[1,0]
	v_pk_mul_f32 v[8:9], v[8:9], v[34:35] op_sel_hi:[1,0]
	v_pk_mul_f32 v[6:7], v[6:7], v[34:35] op_sel_hi:[1,0]
	v_pk_mul_f32 v[4:5], v[4:5], v[34:35] op_sel_hi:[1,0]
	v_pk_mul_f32 v[2:3], v[2:3], v[34:35] op_sel_hi:[1,0]

; __device__ __forceinline__ float xor32_max(float x) { float lo, hi; xor32_pair(x, lo, hi); return fmaxf(lo, hi); }
; #define AT_LDK(dst, kb_i, g_) do { _Pragma("unroll") for (int q_ = 0; q_ < 4; ++q_) dst[q_] = *(const LAS bf16x8*)(kb_ + (kb_i) * 32 * AT_KSTR + (4 * (g_) + q_) * 32); } while (0)
; #define AT_MMK(kb_i, src, g_) do { _Pragma("unroll") for (int q_ = 0; q_ < 4; ++q_) p[kb_i] = __builtin_amdgcn_mfma_f32_32x32x16_bf16(src[q_], qf[4 * (g_) + q_], p[kb_i], 0, 0, 0); } while (0)
; __device__ __forceinline__ void attn_block(Frame& F, int b, int g, int qb, float sbound) {
;     ...
;             for (int kb = 0; kb < 2; ++kb) { const unsigned mword = (kb ? mw.y : mw.x) >> (4 * hi);
; #pragma unroll
;                 for (int r = 0; r < 16; ++r) { const int ko = (r & 3) + 8 * (r >> 2);
;                     const unsigned tm = (unsigned)__builtin_amdgcn_sbfe((int)mword, ko, 1);
;                     p[kb][r] = __builtin_bit_cast(float, (__builtin_bit_cast(unsigned, slope2 * (float)(32 * kb + ko)) & tm) | (__builtin_bit_cast(unsigned, -2e30f) & ~tm)); } }
;             {
;                 bf16x8 ka[4], kc[4];
;     ...
;                 AT_LDK(ka, 0, 0); __builtin_amdgcn_sched_barrier(0); AT_MMK(0, ka, 0); __builtin_amdgcn_sched_barrier(0);
;                 AT_LDK(kc, 0, 1); __builtin_amdgcn_sched_barrier(0); AT_MMK(0, kc, 1); __builtin_amdgcn_sched_barrier(0);
;                 AT_LDK(ka, 1, 0); __builtin_amdgcn_sched_barrier(0); AT_MMK(1, ka, 0); __builtin_amdgcn_sched_barrier(0);
;                 AT_LDK(kc, 1, 1); __builtin_amdgcn_sched_barrier(0); AT_MMK(1, kc, 1); __builtin_amdgcn_sched_barrier(0);
;     ...
;             }
;             const float base = -slope2 * (float)(t - 64 * kt - 4 * hi);
;             float rmax = -3e30f;
; #pragma unroll
;             for (int kb = 0; kb < 2; ++kb)
; #pragma unroll
;                 for (int r = 0; r < 16; ++r) rmax = fmaxf(rmax, p[kb][r]);
;             rmax += base; rmax = xor32_max(rmax);
;             const float mn = fmaxf(m, rmax), alpha = __builtin_amdgcn_exp2f(m - mn), mrel = mn - base;
;             const bool moved = __any(mn != m);
;             m = mn;
.LBB0_1320:
	s_and_b64 vcc, exec, s[34:35]
	s_cbranch_vccnz .LBB0_1324
	s_mul_i32 s0, s46, 0x4400
	s_add_i32 s0, s0, 0
	v_add3_u32 v174, s0, v225, v226
	ds_read_b128 v[176:179], v174
	ds_read_b128 v[232:235], v174 offset:32
	ds_read_b128 v[236:239], v174 offset:64
	ds_read_b128 v[240:243], v174 offset:96
	v_lshrrev_b32_e32 v100, v192, v168
	v_bfe_i32 v116, v100, 0, 1
	v_bfe_i32 v117, v100, 1, 1
	v_bfe_i32 v118, v100, 2, 1
	v_bfe_i32 v119, v100, 3, 1
	v_bfe_i32 v120, v100, 8, 1
	v_bfe_i32 v121, v100, 9, 1
	v_bfe_i32 v122, v100, 10, 1
	v_bfe_i32 v123, v100, 11, 1
	v_bfe_i32 v124, v100, 16, 1
	v_bfe_i32 v125, v100, 17, 1
	v_bfe_i32 v126, v100, 18, 1
	v_bfe_i32 v127, v100, 19, 1
	v_bfe_i32 v128, v100, 24, 1
	v_bfe_i32 v129, v100, 25, 1
	v_bfe_i32 v130, v100, 26, 1
	v_bfe_i32 v131, v100, 27, 1
	v_lshrrev_b32_e32 v100, v192, v169
	v_bfe_i32 v172, v100, 0, 1
	v_bfe_i32 v101, v100, 1, 1
	v_bfe_i32 v102, v100, 2, 1
	v_bfe_i32 v103, v100, 3, 1
	v_bfe_i32 v104, v100, 8, 1
	v_bfe_i32 v105, v100, 9, 1
	v_bfe_i32 v106, v100, 10, 1
	v_bfe_i32 v107, v100, 11, 1
	v_bfe_i32 v108, v100, 16, 1
	v_bfe_i32 v109, v100, 17, 1
	v_bfe_i32 v110, v100, 18, 1
	v_bfe_i32 v111, v100, 19, 1
	v_bfe_i32 v112, v100, 24, 1
	v_bfe_i32 v113, v100, 25, 1
	v_bfe_i32 v114, v100, 26, 1
	v_bfe_i32 v100, v100, 27, 1
	v_bitop3_b32 v131, v217, s50, v131 bitop3:0xe4
	v_bitop3_b32 v130, v216, s50, v130 bitop3:0xe4
	v_bitop3_b32 v129, v215, s50, v129 bitop3:0xe4
	v_bitop3_b32 v128, v214, s50, v128 bitop3:0xe4
	v_bitop3_b32 v127, v213, s50, v127 bitop3:0xe4
	v_bitop3_b32 v126, v212, s50, v126 bitop3:0xe4
	v_bitop3_b32 v125, v211, s50, v125 bitop3:0xe4
	v_bitop3_b32 v124, v210, s50, v124 bitop3:0xe4
	v_bitop3_b32 v123, v209, s50, v123 bitop3:0xe4
	v_bitop3_b32 v122, v208, s50, v122 bitop3:0xe4
	v_bitop3_b32 v121, v207, s50, v121 bitop3:0xe4
	v_bitop3_b32 v120, v206, s50, v120 bitop3:0xe4
	v_bitop3_b32 v119, v205, s50, v119 bitop3:0xe4
	v_bitop3_b32 v118, v204, s50, v118 bitop3:0xe4
	v_bitop3_b32 v117, v1, s50, v117 bitop3:0xe4
	v_bitop3_b32 v116, v50, s50, v116 bitop3:0xe4
	s_waitcnt lgkmcnt(3)
	s_nop 0
	v_mfma_f32_32x32x16_bf16 v[116:131], v[176:179], v[36:39], v[116:131]
	v_bitop3_b32 v115, v33, s50, v100 bitop3:0xe4
	v_bitop3_b32 v114, v32, s50, v114 bitop3:0xe4
	v_bitop3_b32 v113, v31, s50, v113 bitop3:0xe4
	v_bitop3_b32 v112, v30, s50, v112 bitop3:0xe4
	s_waitcnt lgkmcnt(2)
	v_mfma_f32_32x32x16_bf16 v[116:131], v[232:235], v[40:43], v[116:131]
	v_bitop3_b32 v111, v29, s50, v111 bitop3:0xe4
	v_bitop3_b32 v110, v28, s50, v110 bitop3:0xe4
	v_bitop3_b32 v109, v27, s50, v109 bitop3:0xe4
	v_bitop3_b32 v108, v26, s50, v108 bitop3:0xe4
	s_waitcnt lgkmcnt(1)
	v_mfma_f32_32x32x16_bf16 v[116:131], v[236:239], v[44:47], v[116:131]
	v_bitop3_b32 v107, v25, s50, v107 bitop3:0xe4
	v_bitop3_b32 v106, v24, s50, v106 bitop3:0xe4
	v_bitop3_b32 v105, v23, s50, v105 bitop3:0xe4
	v_bitop3_b32 v104, v22, s50, v104 bitop3:0xe4
	s_waitcnt lgkmcnt(0)
	v_mfma_f32_32x32x16_bf16 v[116:131], v[240:243], v[132:135], v[116:131]
	v_bitop3_b32 v103, v21, s50, v103 bitop3:0xe4
	v_bitop3_b32 v102, v20, s50, v102 bitop3:0xe4
	v_bitop3_b32 v101, v19, s50, v101 bitop3:0xe4
	v_bitop3_b32 v100, v18, s50, v172 bitop3:0xe4
	ds_read_b128 v[176:179], v174 offset:128
	ds_read_b128 v[232:235], v174 offset:160
	ds_read_b128 v[236:239], v174 offset:192
	ds_read_b128 v[240:243], v174 offset:224
	s_waitcnt lgkmcnt(3)
	v_mfma_f32_32x32x16_bf16 v[116:131], v[176:179], v[136:139], v[116:131]
	s_waitcnt lgkmcnt(2)
	v_mfma_f32_32x32x16_bf16 v[116:131], v[232:235], v[140:143], v[116:131]
	s_waitcnt lgkmcnt(1)
	v_mfma_f32_32x32x16_bf16 v[116:131], v[236:239], v[144:147], v[116:131]
	s_waitcnt lgkmcnt(0)
	v_mfma_f32_32x32x16_bf16 v[116:131], v[240:243], v[148:151], v[116:131]
	ds_read_b128 v[176:179], v174 offset:8704
	ds_read_b128 v[232:235], v174 offset:8736
	ds_read_b128 v[236:239], v174 offset:8768
	ds_read_b128 v[240:243], v174 offset:8800
	s_waitcnt lgkmcnt(3)
	v_mfma_f32_32x32x16_bf16 v[100:115], v[176:179], v[36:39], v[100:115]
	s_waitcnt lgkmcnt(2)
	v_mfma_f32_32x32x16_bf16 v[100:115], v[232:235], v[40:43], v[100:115]
	s_waitcnt lgkmcnt(1)
	v_mfma_f32_32x32x16_bf16 v[100:115], v[236:239], v[44:47], v[100:115]
	s_waitcnt lgkmcnt(0)
	v_mfma_f32_32x32x16_bf16 v[100:115], v[240:243], v[132:135], v[100:115]
	ds_read_b128 v[176:179], v174 offset:8832
	ds_read_b128 v[232:235], v174 offset:8864
	ds_read_b128 v[236:239], v174 offset:8896
	ds_read_b128 v[240:243], v174 offset:8928
	s_waitcnt lgkmcnt(3)
	v_mfma_f32_32x32x16_bf16 v[100:115], v[176:179], v[136:139], v[100:115]
	s_waitcnt lgkmcnt(2)
	v_mfma_f32_32x32x16_bf16 v[100:115], v[232:235], v[140:143], v[100:115]
	s_waitcnt lgkmcnt(1)
	v_mfma_f32_32x32x16_bf16 v[100:115], v[236:239], v[144:147], v[100:115]
	s_waitcnt lgkmcnt(0)
	v_mfma_f32_32x32x16_bf16 v[100:115], v[240:243], v[148:151], v[100:115]
	v_add_u32_e32 v172, s47, v228
	v_cvt_f32_i32_e32 v176, v172
	v_max3_f32 v172, v116, s51, v117
	v_max3_f32 v172, v172, v118, v119
	v_max3_f32 v172, v172, v120, v121
	v_max3_f32 v172, v172, v122, v123
	v_max3_f32 v172, v172, v124, v125
	v_max3_f32 v172, v172, v126, v127
	v_max3_f32 v172, v172, v128, v129
	v_max3_f32 v172, v172, v130, v131
	s_nop 1
	v_max3_f32 v172, v172, v100, v101
	v_max3_f32 v172, v172, v102, v103
	v_max3_f32 v172, v172, v104, v105
	v_max3_f32 v172, v172, v106, v107
	v_max3_f32 v172, v172, v108, v109
	v_max3_f32 v172, v172, v110, v111
	v_max3_f32 v172, v172, v112, v113
	v_max3_f32 v172, v172, v114, v115
	v_fmac_f32_e32 v172, v220, v176
	v_mov_b32_e32 v174, v172
	s_nop 1
	v_permlane32_swap_b32 v172, v174
	s_nop 0
	v_max3_f32 v174, v175, v172, v174
	v_sub_f32_e32 v172, v175, v174
	v_exp_f32_e32 v172, v172
	v_cmp_neq_f32_e32 vcc, v174, v175
	s_cbranch_vccz .LBB0_1323
; __device__ __forceinline__ void attn_block(Frame& F, int b, int g, int qb, float sbound) {
;     ...
;             if (moved) {
; #pragma unroll
;                 for (int db = 0; db < 4; ++db)
; #pragma unroll
;                     for (int r = 0; r < 16; ++r) o[db][r] *= alpha;
;             }
	v_pk_mul_f32 v[98:99], v[98:99], v[172:173] op_sel_hi:[1,0]
	v_pk_mul_f32 v[96:97], v[96:97], v[172:173] op_sel_hi:[1,0]
	v_pk_mul_f32 v[94:95], v[94:95], v[172:173] op_sel_hi:[1,0]
	v_pk_mul_f32 v[92:93], v[92:93], v[172:173] op_sel_hi:[1,0]
	v_pk_mul_f32 v[90:91], v[90:91], v[172:173] op_sel_hi:[1,0]
	v_pk_mul_f32 v[88:89], v[88:89], v[172:173] op_sel_hi:[1,0]
	v_pk_mul_f32 v[86:87], v[86:87], v[172:173] op_sel_hi:[1,0]
	v_pk_mul_f32 v[84:85], v[84:85], v[172:173] op_sel_hi:[1,0]
	v_pk_mul_f32 v[82:83], v[82:83], v[172:173] op_sel_hi:[1,0]
	v_pk_mul_f32 v[80:81], v[80:81], v[172:173] op_sel_hi:[1,0]
	v_pk_mul_f32 v[78:79], v[78:79], v[172:173] op_sel_hi:[1,0]
	v_pk_mul_f32 v[76:77], v[76:77], v[172:173] op_sel_hi:[1,0]
	v_pk_mul_f32 v[74:75], v[74:75], v[172:173] op_sel_hi:[1,0]
	v_pk_mul_f32 v[72:73], v[72:73], v[172:173] op_sel_hi:[1,0]
	v_pk_mul_f32 v[70:71], v[70:71], v[172:173] op_sel_hi:[1,0]
	v_pk_mul_f32 v[68:69], v[68:69], v[172:173] op_sel_hi:[1,0]
	v_pk_mul_f32 v[66:67], v[66:67], v[172:173] op_sel_hi:[1,0]
	v_pk_mul_f32 v[64:65], v[64:65], v[172:173] op_sel_hi:[1,0]
	v_pk_mul_f32 v[62:63], v[62:63], v[172:173] op_sel_hi:[1,0]
	v_pk_mul_f32 v[60:61], v[60:61], v[172:173] op_sel_hi:[1,0]
	v_pk_mul_f32 v[58:59], v[58:59], v[172:173] op_sel_hi:[1,0]
	v_pk_mul_f32 v[56:57], v[56:57], v[172:173] op_sel_hi:[1,0]
	v_pk_mul_f32 v[54:55], v[54:55], v[172:173] op_sel_hi:[1,0]
	v_pk_mul_f32 v[52:53], v[52:53], v[172:173] op_sel_hi:[1,0]
	v_pk_mul_f32 v[16:17], v[16:17], v[172:173] op_sel_hi:[1,0]
	v_pk_mul_f32 v[14:15], v[14:15], v[172:173] op_sel_hi:[1,0]
	v_pk_mul_f32 v[12:13], v[12:13], v[172:173] op_sel_hi:[1,0]
	v_pk_mul_f32 v[10:11], v[10:11], v[172:173] op_sel_hi:[1,0]
	v_pk_mul_f32 v[8:9], v[8:9], v[172:173] op_sel_hi:[1,0]
	v_pk_mul_f32 v[6:7], v[6:7], v[172:173] op_sel_hi:[1,0]
	v_pk_mul_f32 v[4:5], v[4:5], v[172:173] op_sel_hi:[1,0]
	v_pk_mul_f32 v[2:3], v[2:3], v[172:173] op_sel_hi:[1,0]
